# baseline (speedup 1.0000x reference)
.LBB1_55:
	s_and_b64 vcc, exec, s[4:5]
	s_cbranch_vccz .LBB1_110
	s_and_b32 s72, s2, 7
	s_lshr_b32 s73, s2, 3
	s_mul_i32 s2, s72, 57
	s_add_i32 s2, s2, s73
	s_cmp_lt_u32 s72, 4
	s_cselect_b32 s72, 29, 28
	s_cmp_eq_u32 s73, 28
	s_cselect_b32 s72, 0x100, s72
	s_mov_b32 s73, 0
	s_load_dwordx8 s[8:15], s[0:1], 0x0
	s_load_dwordx2 s[6:7], s[0:1], 0x20
	v_readfirstlane_b32 s3, v0
	s_mov_b32 s29, 41
	s_mov_b32 s0, 0
	s_cmpk_lt_i32 s2, 0x148
	s_mov_b32 s1, 0
	s_cbranch_scc1 .LBB1_62
	s_cmpk_lt_u32 s2, 0x1a0
	s_cbranch_scc1 .LBB1_60
	s_cmpk_lt_u32 s2, 0x1b8
	s_cbranch_scc1 .LBB1_61
	s_cmpk_lt_u32 s2, 0x1c0
	s_movk_i32 s0, 0xfe48
	s_cselect_b32 s1, s0, 0xfffffe40
	s_cselect_b32 s0, 3, 4
	s_mov_b32 s29, 1
	s_branch .LBB1_62

.LBB1_82:
	ds_read_b128 v[130:133], v219 offset:32768
	ds_read_b128 v[134:137], v219 offset:33792
	ds_read_b128 v[138:141], v219 offset:34816
	ds_read_b128 v[142:145], v219 offset:35840
	ds_read_b128 v[146:149], v220
	ds_read_b128 v[150:153], v220 offset:1024
	ds_read_b128 v[154:157], v221
	ds_read_b128 v[158:161], v221 offset:1024
	ds_read_b128 v[162:165], v222
	ds_read_b128 v[166:169], v222 offset:1024
	ds_read_b128 v[170:173], v223
	ds_read_b128 v[174:177], v223 offset:1024
	s_setprio 2
	s_add_i32 s12, s8, 1
	v_readlane_b32 s9, v248, s12
	s_mov_b32 m0, s43
	s_nop 1
	v_add_u32_e32 v129, s9, v249
	global_load_lds_dwordx4 v129, s[18:19]
	v_add_u32_e32 v129, s9, v250
	s_mov_b32 m0, s44
	s_nop 0
	global_load_lds_dwordx4 v129, s[18:19]
	s_setprio 0
	s_waitcnt lgkmcnt(8)
	s_barrier
	s_waitcnt lgkmcnt(0)
	s_setprio 1
	s_waitcnt lgkmcnt(0)
	v_mfma_f32_16x16x32_f16 v[124:127], v[130:133], v[146:149], v[124:127]
	v_mfma_f32_16x16x32_f16 v[120:123], v[138:141], v[146:149], v[120:123]
	v_mfma_f32_16x16x32_f16 v[116:119], v[130:133], v[154:157], v[116:119]
	v_mfma_f32_16x16x32_f16 v[112:115], v[138:141], v[154:157], v[112:115]
	v_mfma_f32_16x16x32_f16 v[108:111], v[130:133], v[162:165], v[108:111]
	v_mfma_f32_16x16x32_f16 v[104:107], v[138:141], v[162:165], v[104:107]
	v_mfma_f32_16x16x32_f16 v[100:103], v[130:133], v[170:173], v[100:103]
	v_mfma_f32_16x16x32_f16 v[96:99], v[138:141], v[170:173], v[96:99]
	v_mfma_f32_16x16x32_f16 v[124:127], v[134:137], v[150:153], v[124:127]
	v_mfma_f32_16x16x32_f16 v[120:123], v[142:145], v[150:153], v[120:123]
	v_mfma_f32_16x16x32_f16 v[116:119], v[134:137], v[158:161], v[116:119]
	v_mfma_f32_16x16x32_f16 v[112:115], v[142:145], v[158:161], v[112:115]
	v_mfma_f32_16x16x32_f16 v[108:111], v[134:137], v[166:169], v[108:111]
	v_mfma_f32_16x16x32_f16 v[104:107], v[142:145], v[166:169], v[104:107]
	v_mfma_f32_16x16x32_f16 v[100:103], v[134:137], v[174:177], v[100:103]
	v_mfma_f32_16x16x32_f16 v[96:99], v[142:145], v[174:177], v[96:99]
	s_setprio 0
	s_barrier
	ds_read_b128 v[178:181], v219 offset:49152
	ds_read_b128 v[182:185], v219 offset:50176
	ds_read_b128 v[186:189], v219 offset:51200
	ds_read_b128 v[190:193], v219 offset:52224
	s_setprio 2
	v_add_u32_e32 v129, s7, v128
	s_mov_b32 m0, s22
	v_add_u32_e32 v194, 0xffffff80, v129
	global_load_lds_dwordx4 v194, s[10:11]
	v_add_u32_e32 v194, 0x47f80, v129
	s_mov_b32 m0, s23
	s_add_i32 s9, s8, 2
	global_load_lds_dwordx4 v194, s[10:11]
	s_setprio 0
	s_barrier
	s_waitcnt lgkmcnt(0)
	s_setprio 1
	s_waitcnt lgkmcnt(0)
	v_mfma_f32_16x16x32_f16 v[52:55], v[178:181], v[146:149], v[52:55]
	v_mfma_f32_16x16x32_f16 v[40:43], v[186:189], v[146:149], v[40:43]
	v_mfma_f32_16x16x32_f16 v[36:39], v[178:181], v[154:157], v[36:39]
	v_mfma_f32_16x16x32_f16 v[32:35], v[186:189], v[154:157], v[32:35]
	v_mfma_f32_16x16x32_f16 v[28:31], v[178:181], v[162:165], v[28:31]
	v_mfma_f32_16x16x32_f16 v[24:27], v[186:189], v[162:165], v[24:27]
	v_mfma_f32_16x16x32_f16 v[20:23], v[178:181], v[170:173], v[20:23]
	v_mfma_f32_16x16x32_f16 v[16:19], v[186:189], v[170:173], v[16:19]
	v_mfma_f32_16x16x32_f16 v[52:55], v[182:185], v[150:153], v[52:55]
	v_mfma_f32_16x16x32_f16 v[40:43], v[190:193], v[150:153], v[40:43]
	v_mfma_f32_16x16x32_f16 v[36:39], v[182:185], v[158:161], v[36:39]
	v_mfma_f32_16x16x32_f16 v[32:35], v[190:193], v[158:161], v[32:35]
	v_mfma_f32_16x16x32_f16 v[28:31], v[182:185], v[166:169], v[28:31]
	v_mfma_f32_16x16x32_f16 v[24:27], v[190:193], v[166:169], v[24:27]
	v_mfma_f32_16x16x32_f16 v[20:23], v[182:185], v[174:177], v[20:23]
	v_mfma_f32_16x16x32_f16 v[16:19], v[190:193], v[174:177], v[16:19]
	s_setprio 0
	s_barrier
	ds_read_b128 v[146:149], v220 offset:16384
	ds_read_b128 v[150:153], v220 offset:17408
	ds_read_b128 v[154:157], v221 offset:16384
	ds_read_b128 v[158:161], v221 offset:17408
	ds_read_b128 v[162:165], v222 offset:16384
	ds_read_b128 v[166:169], v222 offset:17408
	ds_read_b128 v[170:173], v223 offset:16384
	ds_read_b128 v[174:177], v223 offset:17408
	s_setprio 2
	v_readlane_b32 s13, v248, s9
	s_mov_b32 m0, s21
	s_nop 1
	v_add_u32_e32 v194, s13, v206
	global_load_lds_dwordx4 v194, s[18:19]
	v_add_u32_e32 v194, s13, v213
	s_mov_b32 m0, s24
	s_nop 0
	global_load_lds_dwordx4 v194, s[18:19]
	s_setprio 0
	s_barrier
	s_waitcnt lgkmcnt(0)
	s_setprio 1
	s_waitcnt lgkmcnt(0)
	v_mfma_f32_16x16x32_f16 v[12:15], v[130:133], v[146:149], v[12:15]
	v_mfma_f32_16x16x32_f16 v[8:11], v[138:141], v[146:149], v[8:11]
	v_mfma_f32_16x16x32_f16 v[4:7], v[130:133], v[154:157], v[4:7]
	v_mfma_f32_16x16x32_f16 v[0:3], v[138:141], v[154:157], v[0:3]
	v_mfma_f32_16x16x32_f16 v[44:47], v[130:133], v[162:165], v[44:47]
	v_mfma_f32_16x16x32_f16 v[48:51], v[138:141], v[162:165], v[48:51]
	v_mfma_f32_16x16x32_f16 v[56:59], v[130:133], v[170:173], v[56:59]
	v_mfma_f32_16x16x32_f16 v[60:63], v[138:141], v[170:173], v[60:63]
	v_mfma_f32_16x16x32_f16 v[12:15], v[134:137], v[150:153], v[12:15]
	v_mfma_f32_16x16x32_f16 v[8:11], v[142:145], v[150:153], v[8:11]
	v_mfma_f32_16x16x32_f16 v[4:7], v[134:137], v[158:161], v[4:7]
	v_mfma_f32_16x16x32_f16 v[0:3], v[142:145], v[158:161], v[0:3]
	v_mfma_f32_16x16x32_f16 v[44:47], v[134:137], v[166:169], v[44:47]
	v_mfma_f32_16x16x32_f16 v[48:51], v[142:145], v[166:169], v[48:51]
	v_mfma_f32_16x16x32_f16 v[56:59], v[134:137], v[174:177], v[56:59]
	v_mfma_f32_16x16x32_f16 v[60:63], v[142:145], v[174:177], v[60:63]
	s_setprio 0
	s_barrier
	s_setprio 2
	s_mov_b32 m0, s25
	v_add_u32_e32 v130, 0x8ff80, v129
	global_load_lds_dwordx4 v130, s[10:11]
	v_add_u32_e32 v130, 0xd7f80, v129
	s_mov_b32 m0, s26
	s_nop 0
	global_load_lds_dwordx4 v130, s[10:11]
	s_setprio 0
	s_waitcnt vmcnt(6)
	s_barrier
	s_setprio 1
	v_mfma_f32_16x16x32_f16 v[64:67], v[178:181], v[146:149], v[64:67]
	v_mfma_f32_16x16x32_f16 v[68:71], v[186:189], v[146:149], v[68:71]
	v_mfma_f32_16x16x32_f16 v[72:75], v[178:181], v[154:157], v[72:75]
	v_mfma_f32_16x16x32_f16 v[76:79], v[186:189], v[154:157], v[76:79]
	v_mfma_f32_16x16x32_f16 v[80:83], v[178:181], v[162:165], v[80:83]
	v_mfma_f32_16x16x32_f16 v[84:87], v[186:189], v[162:165], v[84:87]
	v_mfma_f32_16x16x32_f16 v[88:91], v[178:181], v[170:173], v[88:91]
	v_mfma_f32_16x16x32_f16 v[92:95], v[186:189], v[170:173], v[92:95]
	v_mfma_f32_16x16x32_f16 v[64:67], v[182:185], v[150:153], v[64:67]
	v_mfma_f32_16x16x32_f16 v[68:71], v[190:193], v[150:153], v[68:71]
	v_mfma_f32_16x16x32_f16 v[72:75], v[182:185], v[158:161], v[72:75]
	v_mfma_f32_16x16x32_f16 v[76:79], v[190:193], v[158:161], v[76:79]
	v_mfma_f32_16x16x32_f16 v[80:83], v[182:185], v[166:169], v[80:83]
	v_mfma_f32_16x16x32_f16 v[84:87], v[190:193], v[166:169], v[84:87]
	v_mfma_f32_16x16x32_f16 v[88:91], v[182:185], v[174:177], v[88:91]
	v_mfma_f32_16x16x32_f16 v[92:95], v[190:193], v[174:177], v[92:95]
	s_setprio 0
	s_barrier
	ds_read_b128 v[130:133], v224
	ds_read_b128 v[134:137], v224 offset:1024
	ds_read_b128 v[138:141], v224 offset:2048
	ds_read_b128 v[142:145], v224 offset:3072
	ds_read_b128 v[146:149], v225
	ds_read_b128 v[150:153], v225 offset:1024
	ds_read_b128 v[154:157], v226
	ds_read_b128 v[158:161], v226 offset:1024
	ds_read_b128 v[162:165], v227
	ds_read_b128 v[166:169], v227 offset:1024
	ds_read_b128 v[170:173], v228
	ds_read_b128 v[174:177], v228 offset:1024
	s_setprio 2
	v_readlane_b32 s12, v248, s9
	s_mov_b32 m0, s27
	s_nop 1
	v_add_u32_e32 v178, s12, v249
	global_load_lds_dwordx4 v178, s[18:19]
	v_add_u32_e32 v178, s12, v250
	s_mov_b32 m0, s28
	s_nop 0
	global_load_lds_dwordx4 v178, s[18:19]
	s_setprio 0
	s_waitcnt lgkmcnt(8)
	s_barrier
	s_waitcnt lgkmcnt(0)
	s_setprio 1
	s_waitcnt lgkmcnt(0)
	v_mfma_f32_16x16x32_f16 v[124:127], v[130:133], v[146:149], v[124:127]
	v_mfma_f32_16x16x32_f16 v[120:123], v[138:141], v[146:149], v[120:123]
	v_mfma_f32_16x16x32_f16 v[116:119], v[130:133], v[154:157], v[116:119]
	v_mfma_f32_16x16x32_f16 v[112:115], v[138:141], v[154:157], v[112:115]
	v_mfma_f32_16x16x32_f16 v[108:111], v[130:133], v[162:165], v[108:111]
	v_mfma_f32_16x16x32_f16 v[104:107], v[138:141], v[162:165], v[104:107]
	v_mfma_f32_16x16x32_f16 v[100:103], v[130:133], v[170:173], v[100:103]
	v_mfma_f32_16x16x32_f16 v[96:99], v[138:141], v[170:173], v[96:99]
	v_mfma_f32_16x16x32_f16 v[124:127], v[134:137], v[150:153], v[124:127]
	v_mfma_f32_16x16x32_f16 v[120:123], v[142:145], v[150:153], v[120:123]
	v_mfma_f32_16x16x32_f16 v[116:119], v[134:137], v[158:161], v[116:119]
	v_mfma_f32_16x16x32_f16 v[112:115], v[142:145], v[158:161], v[112:115]
	v_mfma_f32_16x16x32_f16 v[108:111], v[134:137], v[166:169], v[108:111]
	v_mfma_f32_16x16x32_f16 v[104:107], v[142:145], v[166:169], v[104:107]
	v_mfma_f32_16x16x32_f16 v[100:103], v[134:137], v[174:177], v[100:103]
	v_mfma_f32_16x16x32_f16 v[96:99], v[142:145], v[174:177], v[96:99]
	s_setprio 0
	s_barrier
	ds_read_b128 v[178:181], v229
	ds_read_b128 v[182:185], v229 offset:1024
	ds_read_b128 v[186:189], v229 offset:2048
	ds_read_b128 v[190:193], v229 offset:3072
	s_setprio 2
	s_mov_b32 m0, s37
	v_add_u32_e32 v194, 0x48000, v129
	global_load_lds_dwordx4 v129, s[10:11]
	s_mov_b32 m0, s38
	s_add_i32 s12, s8, 3
	global_load_lds_dwordx4 v194, s[10:11]
	s_setprio 0
	s_barrier
	s_waitcnt lgkmcnt(0)
	s_setprio 1
	s_waitcnt lgkmcnt(0)
	v_mfma_f32_16x16x32_f16 v[52:55], v[178:181], v[146:149], v[52:55]
	v_mfma_f32_16x16x32_f16 v[40:43], v[186:189], v[146:149], v[40:43]
	v_mfma_f32_16x16x32_f16 v[36:39], v[178:181], v[154:157], v[36:39]
	v_mfma_f32_16x16x32_f16 v[32:35], v[186:189], v[154:157], v[32:35]
	v_mfma_f32_16x16x32_f16 v[28:31], v[178:181], v[162:165], v[28:31]
	v_mfma_f32_16x16x32_f16 v[24:27], v[186:189], v[162:165], v[24:27]
	v_mfma_f32_16x16x32_f16 v[20:23], v[178:181], v[170:173], v[20:23]
	v_mfma_f32_16x16x32_f16 v[16:19], v[186:189], v[170:173], v[16:19]
	v_mfma_f32_16x16x32_f16 v[52:55], v[182:185], v[150:153], v[52:55]
	v_mfma_f32_16x16x32_f16 v[40:43], v[190:193], v[150:153], v[40:43]
	v_mfma_f32_16x16x32_f16 v[36:39], v[182:185], v[158:161], v[36:39]
	v_mfma_f32_16x16x32_f16 v[32:35], v[190:193], v[158:161], v[32:35]
	v_mfma_f32_16x16x32_f16 v[28:31], v[182:185], v[166:169], v[28:31]
	v_mfma_f32_16x16x32_f16 v[24:27], v[190:193], v[166:169], v[24:27]
	v_mfma_f32_16x16x32_f16 v[20:23], v[182:185], v[174:177], v[20:23]
	v_mfma_f32_16x16x32_f16 v[16:19], v[190:193], v[174:177], v[16:19]
	s_setprio 0
	s_barrier
	ds_read_b128 v[146:149], v230
	ds_read_b128 v[150:153], v230 offset:1024
	ds_read_b128 v[154:157], v231
	ds_read_b128 v[158:161], v231 offset:1024
	ds_read_b128 v[162:165], v232
	ds_read_b128 v[166:169], v232 offset:1024
	ds_read_b128 v[170:173], v233
	ds_read_b128 v[174:177], v233 offset:1024
	s_setprio 2
	v_readlane_b32 s13, v248, s12
	s_mov_b32 m0, s39
	s_nop 1
	v_add_u32_e32 v194, s13, v206
	global_load_lds_dwordx4 v194, s[18:19]
	v_add_u32_e32 v194, s13, v213
	s_mov_b32 m0, s40
	s_nop 0
	global_load_lds_dwordx4 v194, s[18:19]
	s_setprio 0
	s_barrier
	s_waitcnt lgkmcnt(0)
	s_setprio 1
	s_waitcnt lgkmcnt(0)
	v_mfma_f32_16x16x32_f16 v[12:15], v[130:133], v[146:149], v[12:15]
	v_mfma_f32_16x16x32_f16 v[8:11], v[138:141], v[146:149], v[8:11]
	v_mfma_f32_16x16x32_f16 v[4:7], v[130:133], v[154:157], v[4:7]
	v_mfma_f32_16x16x32_f16 v[0:3], v[138:141], v[154:157], v[0:3]
	v_mfma_f32_16x16x32_f16 v[44:47], v[130:133], v[162:165], v[44:47]
	v_mfma_f32_16x16x32_f16 v[48:51], v[138:141], v[162:165], v[48:51]
	v_mfma_f32_16x16x32_f16 v[56:59], v[130:133], v[170:173], v[56:59]
	v_mfma_f32_16x16x32_f16 v[60:63], v[138:141], v[170:173], v[60:63]
	v_mfma_f32_16x16x32_f16 v[12:15], v[134:137], v[150:153], v[12:15]
	v_mfma_f32_16x16x32_f16 v[8:11], v[142:145], v[150:153], v[8:11]
	v_mfma_f32_16x16x32_f16 v[4:7], v[134:137], v[158:161], v[4:7]
	v_mfma_f32_16x16x32_f16 v[0:3], v[142:145], v[158:161], v[0:3]
	v_mfma_f32_16x16x32_f16 v[44:47], v[134:137], v[166:169], v[44:47]
	v_mfma_f32_16x16x32_f16 v[48:51], v[142:145], v[166:169], v[48:51]
	v_mfma_f32_16x16x32_f16 v[56:59], v[134:137], v[174:177], v[56:59]
	v_mfma_f32_16x16x32_f16 v[60:63], v[142:145], v[174:177], v[60:63]
	s_setprio 0
	s_barrier
	s_setprio 2
	s_mov_b32 m0, s41
	v_add_u32_e32 v130, 0x90000, v129
	global_load_lds_dwordx4 v130, s[10:11]
	v_add_u32_e32 v129, 0xd8000, v129
	s_mov_b32 m0, s42
	s_nop 0
	global_load_lds_dwordx4 v129, s[10:11]
	s_setprio 0
	s_waitcnt vmcnt(6)
	s_barrier
	s_setprio 1
	v_mfma_f32_16x16x32_f16 v[64:67], v[178:181], v[146:149], v[64:67]
	v_mfma_f32_16x16x32_f16 v[68:71], v[186:189], v[146:149], v[68:71]
	v_mfma_f32_16x16x32_f16 v[72:75], v[178:181], v[154:157], v[72:75]
	v_mfma_f32_16x16x32_f16 v[76:79], v[186:189], v[154:157], v[76:79]
	v_mfma_f32_16x16x32_f16 v[80:83], v[178:181], v[162:165], v[80:83]
	v_mfma_f32_16x16x32_f16 v[84:87], v[186:189], v[162:165], v[84:87]
	v_mfma_f32_16x16x32_f16 v[88:91], v[178:181], v[170:173], v[88:91]
	v_mfma_f32_16x16x32_f16 v[92:95], v[186:189], v[170:173], v[92:95]
	v_mfma_f32_16x16x32_f16 v[64:67], v[182:185], v[150:153], v[64:67]
	v_mfma_f32_16x16x32_f16 v[68:71], v[190:193], v[150:153], v[68:71]
	v_mfma_f32_16x16x32_f16 v[72:75], v[182:185], v[158:161], v[72:75]
	v_mfma_f32_16x16x32_f16 v[76:79], v[190:193], v[158:161], v[76:79]
	v_mfma_f32_16x16x32_f16 v[80:83], v[182:185], v[166:169], v[80:83]
	v_mfma_f32_16x16x32_f16 v[84:87], v[190:193], v[166:169], v[84:87]
	v_mfma_f32_16x16x32_f16 v[88:91], v[182:185], v[174:177], v[88:91]
	v_mfma_f32_16x16x32_f16 v[92:95], v[190:193], v[174:177], v[92:95]
	s_setprio 0
	s_addk_i32 s7, 0x100
	s_cmp_lt_u32 s8, 32
	s_mov_b32 s8, s9
	s_barrier
	s_cbranch_scc1 .LBB1_82
	ds_read_b128 v[132:135], v219 offset:32768
	ds_read_b128 v[136:139], v219 offset:33792
	ds_read_b128 v[140:143], v219 offset:34816
	ds_read_b128 v[144:147], v219 offset:35840
	ds_read_b128 v[128:131], v220
	ds_read_b128 v[148:151], v220 offset:1024
	ds_read_b128 v[152:155], v221
	ds_read_b128 v[156:159], v221 offset:1024
	ds_read_b128 v[188:191], v222
	ds_read_b128 v[192:195], v222 offset:1024
	ds_read_b128 v[196:199], v223
	ds_read_b128 v[200:203], v223 offset:1024
	s_setprio 2
	s_lshl_b32 s3, s50, 9
	s_add_i32 s3, s47, s3
	s_add_i32 s3, s3, 0x10380
	s_mov_b32 m0, s43
	v_add_u32_e32 v160, s3, v206
	global_load_lds_dwordx4 v160, s[18:19]
	v_add_u32_e32 v160, s3, v213
	s_mov_b32 m0, s44
	s_nop 0
	global_load_lds_dwordx4 v160, s[18:19]
	s_setprio 0
	s_barrier
	s_waitcnt lgkmcnt(0)
	s_setprio 1
	s_waitcnt lgkmcnt(0)
	v_mfma_f32_16x16x32_f16 v[124:127], v[132:135], v[128:131], v[124:127]
	v_mfma_f32_16x16x32_f16 v[120:123], v[140:143], v[128:131], v[120:123]
	v_mfma_f32_16x16x32_f16 v[116:119], v[132:135], v[152:155], v[116:119]
	v_mfma_f32_16x16x32_f16 v[112:115], v[140:143], v[152:155], v[112:115]
	v_mfma_f32_16x16x32_f16 v[108:111], v[132:135], v[188:191], v[108:111]
	v_mfma_f32_16x16x32_f16 v[104:107], v[140:143], v[188:191], v[104:107]
	v_mfma_f32_16x16x32_f16 v[100:103], v[132:135], v[196:199], v[100:103]
	v_mfma_f32_16x16x32_f16 v[96:99], v[140:143], v[196:199], v[96:99]
	v_mfma_f32_16x16x32_f16 v[160:163], v[136:139], v[148:151], v[124:127]
	v_mfma_f32_16x16x32_f16 v[164:167], v[144:147], v[148:151], v[120:123]
	v_mfma_f32_16x16x32_f16 v[168:171], v[136:139], v[156:159], v[116:119]
	v_mfma_f32_16x16x32_f16 v[172:175], v[144:147], v[156:159], v[112:115]
	v_mfma_f32_16x16x32_f16 v[176:179], v[136:139], v[192:195], v[108:111]
	v_mfma_f32_16x16x32_f16 v[180:183], v[144:147], v[192:195], v[104:107]
	v_mfma_f32_16x16x32_f16 v[100:103], v[136:139], v[200:203], v[100:103]
	v_mfma_f32_16x16x32_f16 v[184:187], v[144:147], v[200:203], v[96:99]
	s_setprio 0
	s_barrier
	ds_read_b128 v[104:107], v219 offset:49152
	ds_read_b128 v[108:111], v219 offset:50176
	ds_read_b128 v[116:119], v219 offset:51200
	ds_read_b128 v[236:239], v219 offset:52224
	s_barrier
	s_waitcnt lgkmcnt(0)
	s_setprio 1
	s_waitcnt lgkmcnt(0)
	v_mfma_f32_16x16x32_f16 v[52:55], v[104:107], v[128:131], v[52:55]
	v_mfma_f32_16x16x32_f16 v[40:43], v[116:119], v[128:131], v[40:43]
	v_mfma_f32_16x16x32_f16 v[36:39], v[104:107], v[152:155], v[36:39]
	v_mfma_f32_16x16x32_f16 v[32:35], v[116:119], v[152:155], v[32:35]
	v_mfma_f32_16x16x32_f16 v[28:31], v[104:107], v[188:191], v[28:31]
	v_mfma_f32_16x16x32_f16 v[24:27], v[116:119], v[188:191], v[24:27]
	v_mfma_f32_16x16x32_f16 v[20:23], v[104:107], v[196:199], v[20:23]
	v_mfma_f32_16x16x32_f16 v[16:19], v[116:119], v[196:199], v[16:19]
	v_mfma_f32_16x16x32_f16 v[52:55], v[108:111], v[148:151], v[52:55]
	v_mfma_f32_16x16x32_f16 v[40:43], v[236:239], v[148:151], v[40:43]
	v_mfma_f32_16x16x32_f16 v[36:39], v[108:111], v[156:159], v[36:39]
	v_mfma_f32_16x16x32_f16 v[32:35], v[236:239], v[156:159], v[32:35]
	v_mfma_f32_16x16x32_f16 v[28:31], v[108:111], v[192:195], v[28:31]
	v_mfma_f32_16x16x32_f16 v[24:27], v[236:239], v[192:195], v[24:27]
	v_mfma_f32_16x16x32_f16 v[96:99], v[108:111], v[200:203], v[20:23]
	v_mfma_f32_16x16x32_f16 v[16:19], v[236:239], v[200:203], v[16:19]
	s_setprio 0
	s_barrier
	ds_read_b128 v[20:23], v220 offset:16384
	ds_read_b128 v[148:151], v220 offset:17408
	ds_read_b128 v[152:155], v221 offset:16384
	ds_read_b128 v[156:159], v221 offset:17408
	ds_read_b128 v[188:191], v222 offset:16384
	ds_read_b128 v[192:195], v222 offset:17408
	ds_read_b128 v[196:199], v223 offset:16384
	ds_read_b128 v[200:203], v223 offset:17408
	s_waitcnt vmcnt(4)
	s_barrier
	s_waitcnt lgkmcnt(0)
	s_setprio 1
	s_waitcnt lgkmcnt(0)
	v_mfma_f32_16x16x32_f16 v[0:3], v[140:143], v[152:155], v[0:3]
	v_mfma_f32_16x16x32_f16 v[124:127], v[144:147], v[156:159], v[0:3]
	v_mfma_f32_16x16x32_f16 v[0:3], v[132:135], v[188:191], v[44:47]
	v_mfma_f32_16x16x32_f16 v[128:131], v[136:139], v[192:195], v[0:3]
	v_mfma_f32_16x16x32_f16 v[0:3], v[140:143], v[188:191], v[48:51]
	v_mfma_f32_16x16x32_f16 v[48:51], v[144:147], v[192:195], v[0:3]
	v_mfma_f32_16x16x32_f16 v[0:3], v[132:135], v[196:199], v[56:59]
	v_mfma_f32_16x16x32_f16 v[12:15], v[132:135], v[20:23], v[12:15]
	v_mfma_f32_16x16x32_f16 v[8:11], v[140:143], v[20:23], v[8:11]
	v_mfma_f32_16x16x32_f16 v[4:7], v[132:135], v[152:155], v[4:7]
	v_mfma_f32_16x16x32_f16 v[56:59], v[136:139], v[200:203], v[0:3]
	v_mfma_f32_16x16x32_f16 v[0:3], v[140:143], v[196:199], v[60:63]
	v_mfma_f32_16x16x32_f16 v[112:115], v[136:139], v[148:151], v[12:15]
	v_mfma_f32_16x16x32_f16 v[8:11], v[144:147], v[148:151], v[8:11]
	v_mfma_f32_16x16x32_f16 v[120:123], v[136:139], v[156:159], v[4:7]
	v_mfma_f32_16x16x32_f16 v[60:63], v[144:147], v[200:203], v[0:3]
	s_setprio 0
	s_setprio 1
	v_mfma_f32_16x16x32_f16 v[0:3], v[104:107], v[20:23], v[64:67]
	v_mfma_f32_16x16x32_f16 v[132:135], v[108:111], v[148:151], v[0:3]
	v_mfma_f32_16x16x32_f16 v[0:3], v[116:119], v[20:23], v[68:71]
	v_mfma_f32_16x16x32_f16 v[136:139], v[236:239], v[148:151], v[0:3]
	v_mfma_f32_16x16x32_f16 v[0:3], v[104:107], v[152:155], v[72:75]
	v_mfma_f32_16x16x32_f16 v[140:143], v[108:111], v[156:159], v[0:3]
	v_mfma_f32_16x16x32_f16 v[0:3], v[116:119], v[152:155], v[76:79]
	v_mfma_f32_16x16x32_f16 v[144:147], v[236:239], v[156:159], v[0:3]
	v_mfma_f32_16x16x32_f16 v[0:3], v[104:107], v[188:191], v[80:83]
	v_mfma_f32_16x16x32_f16 v[80:83], v[108:111], v[192:195], v[0:3]
	v_mfma_f32_16x16x32_f16 v[0:3], v[116:119], v[188:191], v[84:87]
	v_mfma_f32_16x16x32_f16 v[148:151], v[236:239], v[192:195], v[0:3]
	v_mfma_f32_16x16x32_f16 v[0:3], v[104:107], v[196:199], v[88:91]
	v_mfma_f32_16x16x32_f16 v[152:155], v[108:111], v[200:203], v[0:3]
	v_mfma_f32_16x16x32_f16 v[0:3], v[116:119], v[196:199], v[92:95]
	v_mfma_f32_16x16x32_f16 v[156:159], v[236:239], v[200:203], v[0:3]
	s_setprio 0
	s_add_i32 s49, s49, s72
	s_cmp_lt_i32 s73, 1
	s_cselect_b64 s[6:7], -1, 0
	s_cmp_gt_i32 s73, 0
	s_cselect_b64 s[12:13], -1, 0
	s_add_i32 s73, s73, 1
	s_and_b64 vcc, exec, s[12:13]
	s_mov_b32 s54, s2
	s_mov_b32 s53, s51
	s_mov_b32 s55, s52
	s_barrier
	s_cbranch_vccnz .LBB1_100
	s_cmpk_lt_i32 s49, 0x148
	s_cbranch_scc1 .LBB1_88
	s_cmpk_lt_u32 s49, 0x1a0
	s_cbranch_scc1 .LBB1_89
	s_cmpk_lt_u32 s49, 0x1b8
	s_cbranch_scc1 .LBB1_90
	s_cmpk_lt_u32 s49, 0x1c0
	s_cselect_b32 s47, s45, 0xfffffe40
	s_cselect_b32 s48, 3, 4
	s_mov_b32 s3, 1
	s_cmp_lt_i32 s48, 1
	s_movk_i32 s53, 0x64
	s_cbranch_scc0 .LBB1_91
	s_branch .LBB1_99

	.amdhsa_kernel _Z9conv_gemmPKDF16_S0_PKfPDF16_PfiiS3_S2_iS2_S2_
		.amdhsa_group_segment_fixed_size 0
		.amdhsa_private_segment_fixed_size 0
		.amdhsa_kernarg_size 344
		.amdhsa_user_sgpr_count 2
		.amdhsa_user_sgpr_dispatch_ptr 0
		.amdhsa_user_sgpr_queue_ptr 0
		.amdhsa_user_sgpr_kernarg_segment_ptr 1
		.amdhsa_user_sgpr_dispatch_id 0
		.amdhsa_user_sgpr_kernarg_preload_length 0
		.amdhsa_user_sgpr_kernarg_preload_offset 0
		.amdhsa_user_sgpr_private_segment_size 0
		.amdhsa_uses_dynamic_stack 0
		.amdhsa_enable_private_segment 0
		.amdhsa_system_sgpr_workgroup_id_x 1
		.amdhsa_system_sgpr_workgroup_id_y 0
		.amdhsa_system_sgpr_workgroup_id_z 0
		.amdhsa_system_sgpr_workgroup_info 0
		.amdhsa_system_vgpr_workitem_id 0
		.amdhsa_next_free_vgpr 256
		.amdhsa_next_free_sgpr 74
		.amdhsa_accum_offset 256
		.amdhsa_reserve_vcc 1
		.amdhsa_float_round_mode_32 0
		.amdhsa_float_round_mode_16_64 0
		.amdhsa_float_denorm_mode_32 3
		.amdhsa_float_denorm_mode_16_64 3
		.amdhsa_dx10_clamp 1
		.amdhsa_ieee_mode 1
		.amdhsa_fp16_overflow 0
		.amdhsa_tg_split 0
		.amdhsa_exception_fp_ieee_invalid_op 0
		.amdhsa_exception_fp_denorm_src 0
		.amdhsa_exception_fp_ieee_div_zero 0
		.amdhsa_exception_fp_ieee_overflow 0
		.amdhsa_exception_fp_ieee_underflow 0
		.amdhsa_exception_fp_ieee_inexact 0
		.amdhsa_exception_int_div_zero 0
	.end_amdhsa_kernel

amdhsa.kernels:
  - .agpr_count:     0
    .args:
      - .offset:         0
        .size:           40
        .value_kind:     by_value
      - .actual_access:  read_only
        .address_space:  global
        .offset:         40
        .size:           8
        .value_kind:     global_buffer
      - .actual_access:  read_only
        .address_space:  global
        .offset:         48
        .size:           8
        .value_kind:     global_buffer
      - .actual_access:  read_only
        .address_space:  global
        .offset:         56
        .size:           8
        .value_kind:     global_buffer
      - .actual_access:  read_only
        .address_space:  global
        .offset:         64
        .size:           8
        .value_kind:     global_buffer
      - .actual_access:  read_only
        .address_space:  global
        .offset:         72
        .size:           8
        .value_kind:     global_buffer
      - .actual_access:  write_only
        .address_space:  global
        .offset:         80
        .size:           8
        .value_kind:     global_buffer
      - .actual_access:  write_only
        .address_space:  global
        .offset:         88
        .size:           8
        .value_kind:     global_buffer
      - .actual_access:  write_only
        .address_space:  global
        .offset:         96
        .size:           8
        .value_kind:     global_buffer
    .group_segment_fixed_size: 16384
    .kernarg_segment_align: 8
    .kernarg_segment_size: 104
    .language:       OpenCL C
    .language_version:
      - 2
      - 0
    .max_flat_workgroup_size: 256
    .name:           _Z8prep_all8FeatPtrsPKfS1_S1_S1_S1_PDF16_S2_S2_
    .private_segment_fixed_size: 0
    .sgpr_count:     26
    .sgpr_spill_count: 0
    .symbol:         _Z8prep_all8FeatPtrsPKfS1_S1_S1_S1_PDF16_S2_S2_.kd
    .uniform_work_group_size: 1
    .uses_dynamic_stack: false
    .vgpr_count:     38
    .vgpr_spill_count: 0
    .wavefront_size: 64
  - .agpr_count:     0
    .args:
      - .address_space:  global
        .offset:         0
        .size:           8
        .value_kind:     global_buffer
      - .address_space:  global
        .offset:         8
        .size:           8
        .value_kind:     global_buffer
      - .actual_access:  read_only
        .address_space:  global
        .offset:         16
        .size:           8
        .value_kind:     global_buffer
      - .actual_access:  write_only
        .address_space:  global
        .offset:         24
        .size:           8
        .value_kind:     global_buffer
      - .actual_access:  write_only
        .address_space:  global
        .offset:         32
        .size:           8
        .value_kind:     global_buffer
      - .offset:         40
        .size:           4
        .value_kind:     by_value
      - .offset:         44
        .size:           4
        .value_kind:     by_value
      - .address_space:  global
        .offset:         48
        .size:           8
        .value_kind:     global_buffer
      - .actual_access:  read_only
        .address_space:  global
        .offset:         56
        .size:           8
        .value_kind:     global_buffer
      - .offset:         64
        .size:           4
        .value_kind:     by_value
      - .actual_access:  read_only
        .address_space:  global
        .offset:         72
        .size:           8
        .value_kind:     global_buffer
      - .actual_access:  read_only
        .address_space:  global
        .offset:         80
        .size:           8
        .value_kind:     global_buffer
      - .offset:         88
        .size:           4
        .value_kind:     hidden_block_count_x
      - .offset:         92
        .size:           4
        .value_kind:     hidden_block_count_y
      - .offset:         96
        .size:           4
        .value_kind:     hidden_block_count_z
      - .offset:         100
        .size:           2
        .value_kind:     hidden_group_size_x
      - .offset:         102
        .size:           2
        .value_kind:     hidden_group_size_y
      - .offset:         104
        .size:           2
        .value_kind:     hidden_group_size_z
      - .offset:         106
        .size:           2
        .value_kind:     hidden_remainder_x
      - .offset:         108
        .size:           2
        .value_kind:     hidden_remainder_y
      - .offset:         110
        .size:           2
        .value_kind:     hidden_remainder_z
      - .offset:         128
        .size:           8
        .value_kind:     hidden_global_offset_x
      - .offset:         136
        .size:           8
        .value_kind:     hidden_global_offset_y
      - .offset:         144
        .size:           8
        .value_kind:     hidden_global_offset_z
      - .offset:         152
        .size:           2
        .value_kind:     hidden_grid_dims
      - .offset:         208
        .size:           4
        .value_kind:     hidden_dynamic_lds_size
    .group_segment_fixed_size: 0
    .kernarg_segment_align: 8
    .kernarg_segment_size: 344
    .language:       OpenCL C
    .language_version:
      - 2
      - 0
    .max_flat_workgroup_size: 512
    .name:           _Z9conv_gemmPKDF16_S0_PKfPDF16_PfiiS3_S2_iS2_S2_
    .private_segment_fixed_size: 0
    .sgpr_count:     80
    .sgpr_spill_count: 0
    .symbol:         _Z9conv_gemmPKDF16_S0_PKfPDF16_PfiiS3_S2_iS2_S2_.kd
    .uniform_work_group_size: 1
    .uses_dynamic_stack: false
    .vgpr_count:     256
    .vgpr_spill_count: 0
    .wavefront_size: 64
  - .agpr_count:     0
    .args:
      - .actual_access:  read_only
        .address_space:  global
        .offset:         0
        .size:           8
        .value_kind:     global_buffer
      - .actual_access:  read_only
        .address_space:  global
        .offset:         8
        .size:           8
        .value_kind:     global_buffer
      - .actual_access:  read_only
        .address_space:  global
        .offset:         16
        .size:           8
        .value_kind:     global_buffer
      - .actual_access:  read_only
        .address_space:  global
        .offset:         24
        .size:           8
        .value_kind:     global_buffer
      - .actual_access:  read_only
        .address_space:  global
        .offset:         32
        .size:           8
        .value_kind:     global_buffer
      - .actual_access:  read_only
        .address_space:  global
        .offset:         40
        .size:           8
        .value_kind:     global_buffer
      - .actual_access:  read_only
        .address_space:  global
        .offset:         48
        .size:           8
        .value_kind:     global_buffer
      - .actual_access:  read_only
        .address_space:  global
        .offset:         56
        .size:           8
        .value_kind:     global_buffer
      - .actual_access:  read_only
        .address_space:  global
        .offset:         64
        .size:           8
        .value_kind:     global_buffer
      - .actual_access:  read_only
        .address_space:  global
        .offset:         72
        .size:           8
        .value_kind:     global_buffer
      - .actual_access:  read_only
        .address_space:  global
        .offset:         80
        .size:           8
        .value_kind:     global_buffer
      - .actual_access:  write_only
        .address_space:  global
        .offset:         88
        .size:           8
        .value_kind:     global_buffer
    .group_segment_fixed_size: 49152
    .kernarg_segment_align: 8
    .kernarg_segment_size: 96
    .language:       OpenCL C
    .language_version:
      - 2
      - 0
    .max_flat_workgroup_size: 512
    .name:           _Z10head_fusedPKDF16_S0_S0_PKfS2_S2_S2_S2_S2_S2_S2_Pf
    .private_segment_fixed_size: 0
    .sgpr_count:     57
    .sgpr_spill_count: 0
    .symbol:         _Z10head_fusedPKDF16_S0_S0_PKfS2_S2_S2_S2_S2_S2_S2_Pf.kd
    .uniform_work_group_size: 1
    .uses_dynamic_stack: false
    .vgpr_count:     94
    .vgpr_spill_count: 0
    .wavefront_size: 64
